# grid barrier: all workgroups wait on the cross-XCD arrival counter reaching (gen+1)*nx instead of the separately written generation word; on top of flat release
# speedup vs baseline: 1.0054x; 1.0024x over previous
; __device__ __forceinline__ unsigned xb_ld(unsigned* p)              { return __hip_atomic_load(p, __ATOMIC_RELAXED, __HIP_MEMORY_SCOPE_AGENT); }
; __device__ __forceinline__ unsigned xb_add(unsigned* p, unsigned v) { return __hip_atomic_fetch_add(p, v, __ATOMIC_RELAXED, __HIP_MEMORY_SCOPE_AGENT); }
; #define XB_SPIN(cond, bar) do { unsigned _sp = 0; while (cond) { __builtin_amdgcn_s_sleep(1); \
;     if ((++_sp & 255u) == 0u) { if (xb_ld(&(bar)[XB_TMO])) break; if (_sp > XB_SPIN_CAP) { atomicAdd(&(bar)[XB_TMO], 1u); break; } } } } while (0)
; __device__ __forceinline__ void xcd_barrier(const XcdBarrier& b) {
;     ...
;         const unsigned gen = old / nloc;
;         if (old + 1u == (gen + 1u) * nloc) {
;             __builtin_amdgcn_fence(__ATOMIC_RELEASE, "agent");
;             asm volatile("s_waitcnt vmcnt(0)" ::: "memory");
;             const unsigned og = xb_add(&bar[XB_TOP], 1u);
;             const unsigned tg = og / nx;
;             if (og + 1u == (tg + 1u) * nx) xb_add(&bar[XB_TOPGEN], 1u);
;             else XB_SPIN(xb_ld(&bar[XB_TOPGEN]) == tg, bar);
;             __builtin_amdgcn_fence(__ATOMIC_ACQUIRE, "agent");
;             xb_add(&bar[XB_XGEN(b.x)], 1u);
;             asm volatile("s_waitcnt vmcnt(0)" ::: "memory");
;         } else {
;             XB_SPIN(xb_ld(&bar[XB_XGEN(b.x)]) == gen, bar);
.LBB0_124:
	s_or_b64 exec, exec, s[28:29]
	v_cvt_f32_u32_e32 v5, v3
	s_waitcnt vmcnt(1)
	v_readfirstlane_b32 s10, v4
	v_sub_u32_e32 v4, 0, v3
	v_rcp_iflag_f32_e32 v5, v5
	v_add_u32_e32 v6, s10, v2
	v_mul_f32_e32 v5, 0x4f7ffffe, v5
	v_cvt_u32_f32_e32 v5, v5
	v_mul_lo_u32 v2, v4, v5
	v_mul_hi_u32 v2, v5, v2
	v_add_u32_e32 v2, v5, v2
	v_mul_hi_u32 v2, v6, v2
	v_mul_lo_u32 v4, v2, v3
	v_sub_u32_e32 v4, v6, v4
	v_add_u32_e32 v5, 1, v2
	v_cmp_ge_u32_e32 vcc, v4, v3
	s_nop 1
	v_cndmask_b32_e32 v2, v2, v5, vcc
	v_sub_u32_e32 v5, v4, v3
	v_cndmask_b32_e32 v4, v4, v5, vcc
	v_add_u32_e32 v5, 1, v2
	v_cmp_ge_u32_e32 vcc, v4, v3
	v_add_u32_e32 v4, 1, v6
	s_nop 0
	v_cndmask_b32_e32 v2, v2, v5, vcc
	v_mul_lo_u32 v5, v3, v2
	v_add_u32_e32 v3, v5, v3
	v_cmp_ne_u32_e32 vcc, v4, v3
	s_and_saveexec_b64 s[10:11], vcc
	s_xor_b64 s[10:11], exec, s[10:11]
	s_cbranch_execz .LBB0_138
	s_waitcnt lgkmcnt(0)
	v_mov_b32_e32 v20, 0x23824
	ds_read_b32 v20, v20
	v_add_u32_e32 v21, 1, v2
	s_waitcnt lgkmcnt(0)
	v_mul_lo_u32 v21, v21, v20
	v_mov_b32_e32 v1, 0
	s_lshl_b32 s99, s33, 8
	s_sub_u32 s34, s8, s99
	s_subb_u32 s35, s9, 0
	s_add_u32 s34, s34, 0x3400
	s_addc_u32 s35, s35, 0
	global_load_dword v1, v1, s[34:35] sc1
	s_waitcnt vmcnt(0)
	v_cmp_lt_u32_e32 vcc, v1, v21
	s_and_saveexec_b64 s[28:29], vcc
	s_cbranch_execz .LBB0_137
	s_add_u32 s30, s22, 0x4200
	s_addc_u32 s31, s23, 0
	s_mov_b32 s14, 1
	s_mov_b64 s[36:37], 0
	v_mov_b32_e32 v1, 0
	s_branch .LBB0_128

.LBB0_130:
	global_load_dword v3, v1, s[34:35] sc1
	s_add_i32 s14, s14, 1
	s_mov_b64 s[42:43], -1
	s_waitcnt vmcnt(0)
	v_cmp_ge_u32_e32 vcc, v3, v21
	s_orn2_b64 s[40:41], vcc, exec
	s_branch .LBB0_127

; __device__ __forceinline__ unsigned xb_ld(unsigned* p)              { return __hip_atomic_load(p, __ATOMIC_RELAXED, __HIP_MEMORY_SCOPE_AGENT); }
; __device__ __forceinline__ unsigned xb_add(unsigned* p, unsigned v) { return __hip_atomic_fetch_add(p, v, __ATOMIC_RELAXED, __HIP_MEMORY_SCOPE_AGENT); }
; #define XB_SPIN(cond, bar) do { unsigned _sp = 0; while (cond) { __builtin_amdgcn_s_sleep(1); \
;     if ((++_sp & 255u) == 0u) { if (xb_ld(&(bar)[XB_TMO])) break; if (_sp > XB_SPIN_CAP) { atomicAdd(&(bar)[XB_TMO], 1u); break; } } } } while (0)
; __device__ __forceinline__ void xcd_barrier(const XcdBarrier& b) {
;     ...
;             const unsigned og = xb_add(&bar[XB_TOP], 1u);
;             const unsigned tg = og / nx;
;             if (og + 1u == (tg + 1u) * nx) xb_add(&bar[XB_TOPGEN], 1u);
;             else XB_SPIN(xb_ld(&bar[XB_TOPGEN]) == tg, bar);
.LBB0_141:
	s_or_b64 exec, exec, s[28:29]
	v_cvt_f32_u32_e32 v4, v1
	s_waitcnt vmcnt(0)
	v_readfirstlane_b32 s10, v3
	s_add_u32 s28, s22, 0x7500
	s_addc_u32 s29, s23, 0
	v_rcp_iflag_f32_e32 v4, v4
	v_add_u32_e32 v2, s10, v2
	v_add_u32_e32 v5, 1, v2
	s_mov_b64 s[30:31], -1
	v_mul_f32_e32 v3, 0x4f7ffffe, v4
	v_cvt_u32_f32_e32 v3, v3
	v_sub_u32_e32 v4, 0, v1
	v_mul_lo_u32 v4, v4, v3
	v_mul_hi_u32 v4, v3, v4
	v_add_u32_e32 v3, v3, v4
	v_mul_hi_u32 v3, v2, v3
	v_mul_lo_u32 v4, v3, v1
	v_sub_u32_e32 v2, v2, v4
	v_add_u32_e32 v6, 1, v3
	v_cmp_ge_u32_e32 vcc, v2, v1
	v_sub_u32_e32 v4, v2, v1
	s_nop 0
	v_cndmask_b32_e32 v3, v3, v6, vcc
	v_cndmask_b32_e32 v2, v2, v4, vcc
	v_add_u32_e32 v4, 1, v3
	v_cmp_ge_u32_e32 vcc, v2, v1
	s_nop 1
	v_cndmask_b32_e32 v4, v3, v4, vcc
	v_mul_lo_u32 v2, v1, v4
	v_add_u32_e32 v1, v2, v1
	v_mov_b32_e32 v19, v1
	v_cmp_ne_u32_e32 vcc, v5, v1
	v_mov_b64_e32 v[2:3], s[28:29]
	s_and_saveexec_b64 s[10:11], vcc
	s_cbranch_execz .LBB0_153
	v_mov_b32_e32 v1, 0
	global_load_dword v2, v1, s[28:29] offset:-256 sc1
	s_mov_b64 s[36:37], 0
	s_waitcnt vmcnt(0)
	v_cmp_lt_u32_e32 vcc, v2, v19
	s_and_saveexec_b64 s[34:35], vcc
	s_cbranch_execz .LBB0_152
	s_add_u32 s30, s22, 0x4200
	s_addc_u32 s31, s23, 0
	s_mov_b32 s14, 1
	s_branch .LBB0_145

.LBB0_147:
	global_load_dword v2, v1, s[28:29] offset:-256 sc1
	s_add_i32 s14, s14, 1
	s_mov_b64 s[40:41], -1
	s_waitcnt vmcnt(0)
	v_cmp_ge_u32_e32 vcc, v2, v19
	s_orn2_b64 s[44:45], vcc, exec
	s_branch .LBB0_144

; __device__ __forceinline__ unsigned xb_ld(unsigned* p)              { return __hip_atomic_load(p, __ATOMIC_RELAXED, __HIP_MEMORY_SCOPE_AGENT); }
; __device__ __forceinline__ unsigned xb_add(unsigned* p, unsigned v) { return __hip_atomic_fetch_add(p, v, __ATOMIC_RELAXED, __HIP_MEMORY_SCOPE_AGENT); }
; #define XB_SPIN(cond, bar) do { unsigned _sp = 0; while (cond) { __builtin_amdgcn_s_sleep(1); \
;     if ((++_sp & 255u) == 0u) { if (xb_ld(&(bar)[XB_TMO])) break; if (_sp > XB_SPIN_CAP) { atomicAdd(&(bar)[XB_TMO], 1u); break; } } } } while (0)
; __device__ __forceinline__ void xcd_barrier(const XcdBarrier& b) {
;     ...
;         const unsigned gen = old / nloc;
;         if (old + 1u == (gen + 1u) * nloc) {
;             __builtin_amdgcn_fence(__ATOMIC_RELEASE, "agent");
;             asm volatile("s_waitcnt vmcnt(0)" ::: "memory");
;             const unsigned og = xb_add(&bar[XB_TOP], 1u);
;             const unsigned tg = og / nx;
;             if (og + 1u == (tg + 1u) * nx) xb_add(&bar[XB_TOPGEN], 1u);
;             else XB_SPIN(xb_ld(&bar[XB_TOPGEN]) == tg, bar);
;             __builtin_amdgcn_fence(__ATOMIC_ACQUIRE, "agent");
;             xb_add(&bar[XB_XGEN(b.x)], 1u);
;             asm volatile("s_waitcnt vmcnt(0)" ::: "memory");
;         } else {
;             XB_SPIN(xb_ld(&bar[XB_XGEN(b.x)]) == gen, bar);
.LBB0_906:
	s_or_b64 exec, exec, s[10:11]
	v_cvt_f32_u32_e32 v5, v3
	s_waitcnt vmcnt(1)
	v_readfirstlane_b32 s8, v4
	v_sub_u32_e32 v4, 0, v3
	v_rcp_iflag_f32_e32 v5, v5
	v_add_u32_e32 v6, s8, v2
	v_mul_f32_e32 v5, 0x4f7ffffe, v5
	v_cvt_u32_f32_e32 v5, v5
	v_mul_lo_u32 v2, v4, v5
	v_mul_hi_u32 v2, v5, v2
	v_add_u32_e32 v2, v5, v2
	v_mul_hi_u32 v2, v6, v2
	v_mul_lo_u32 v4, v2, v3
	v_sub_u32_e32 v4, v6, v4
	v_add_u32_e32 v5, 1, v2
	v_cmp_ge_u32_e32 vcc, v4, v3
	s_nop 1
	v_cndmask_b32_e32 v2, v2, v5, vcc
	v_sub_u32_e32 v5, v4, v3
	v_cndmask_b32_e32 v4, v4, v5, vcc
	v_add_u32_e32 v5, 1, v2
	v_cmp_ge_u32_e32 vcc, v4, v3
	v_add_u32_e32 v4, 1, v6
	s_nop 0
	v_cndmask_b32_e32 v2, v2, v5, vcc
	v_mul_lo_u32 v5, v3, v2
	v_add_u32_e32 v3, v5, v3
	v_cmp_ne_u32_e32 vcc, v4, v3
	s_and_saveexec_b64 s[8:9], vcc
	s_xor_b64 s[8:9], exec, s[8:9]
	s_cbranch_execz .LBB0_920
	s_waitcnt lgkmcnt(0)
	v_mov_b32_e32 v20, 0x23834
	ds_read_b32 v20, v20
	v_add_u32_e32 v21, 1, v2
	s_waitcnt lgkmcnt(0)
	v_mul_lo_u32 v21, v21, v20
	v_mov_b32_e32 v1, 0
	s_lshl_b32 s99, s33, 8
	s_sub_u32 s16, s6, s99
	s_subb_u32 s17, s7, 0
	s_add_u32 s16, s16, 0x3400
	s_addc_u32 s17, s17, 0
	global_load_dword v1, v1, s[16:17] sc1
	s_waitcnt vmcnt(0)
	v_cmp_lt_u32_e32 vcc, v1, v21
	s_and_saveexec_b64 s[10:11], vcc
	s_cbranch_execz .LBB0_919
	s_add_u32 s12, s22, 0xc200
	s_addc_u32 s13, s23, 0
	s_mov_b32 s14, 1
	s_mov_b64 s[28:29], 0
	v_mov_b32_e32 v1, 0
	s_branch .LBB0_910

.LBB0_912:
	global_load_dword v3, v1, s[16:17] sc1
	s_add_i32 s14, s14, 1
	s_mov_b64 s[36:37], -1
	s_waitcnt vmcnt(0)
	v_cmp_ge_u32_e32 vcc, v3, v21
	s_orn2_b64 s[34:35], vcc, exec
	s_branch .LBB0_909

; __device__ __forceinline__ unsigned xb_ld(unsigned* p)              { return __hip_atomic_load(p, __ATOMIC_RELAXED, __HIP_MEMORY_SCOPE_AGENT); }
; __device__ __forceinline__ unsigned xb_add(unsigned* p, unsigned v) { return __hip_atomic_fetch_add(p, v, __ATOMIC_RELAXED, __HIP_MEMORY_SCOPE_AGENT); }
; #define XB_SPIN(cond, bar) do { unsigned _sp = 0; while (cond) { __builtin_amdgcn_s_sleep(1); \
;     if ((++_sp & 255u) == 0u) { if (xb_ld(&(bar)[XB_TMO])) break; if (_sp > XB_SPIN_CAP) { atomicAdd(&(bar)[XB_TMO], 1u); break; } } } } while (0)
; __device__ __forceinline__ void xcd_barrier(const XcdBarrier& b) {
;     ...
;             const unsigned og = xb_add(&bar[XB_TOP], 1u);
;             const unsigned tg = og / nx;
;             if (og + 1u == (tg + 1u) * nx) xb_add(&bar[XB_TOPGEN], 1u);
;             else XB_SPIN(xb_ld(&bar[XB_TOPGEN]) == tg, bar);
.LBB0_923:
	s_or_b64 exec, exec, s[10:11]
	v_cvt_f32_u32_e32 v4, v1
	s_waitcnt vmcnt(0)
	v_readfirstlane_b32 s8, v3
	s_add_u32 s10, s22, 0xf500
	s_addc_u32 s11, s23, 0
	v_rcp_iflag_f32_e32 v4, v4
	v_add_u32_e32 v2, s8, v2
	v_add_u32_e32 v5, 1, v2
	s_mov_b64 s[12:13], -1
	v_mul_f32_e32 v3, 0x4f7ffffe, v4
	v_cvt_u32_f32_e32 v3, v3
	v_sub_u32_e32 v4, 0, v1
	v_mul_lo_u32 v4, v4, v3
	v_mul_hi_u32 v4, v3, v4
	v_add_u32_e32 v3, v3, v4
	v_mul_hi_u32 v3, v2, v3
	v_mul_lo_u32 v4, v3, v1
	v_sub_u32_e32 v2, v2, v4
	v_add_u32_e32 v6, 1, v3
	v_cmp_ge_u32_e32 vcc, v2, v1
	v_sub_u32_e32 v4, v2, v1
	s_nop 0
	v_cndmask_b32_e32 v3, v3, v6, vcc
	v_cndmask_b32_e32 v2, v2, v4, vcc
	v_add_u32_e32 v4, 1, v3
	v_cmp_ge_u32_e32 vcc, v2, v1
	s_nop 1
	v_cndmask_b32_e32 v4, v3, v4, vcc
	v_mul_lo_u32 v2, v1, v4
	v_add_u32_e32 v1, v2, v1
	v_mov_b32_e32 v19, v1
	v_cmp_ne_u32_e32 vcc, v5, v1
	v_mov_b64_e32 v[2:3], s[10:11]
	s_and_saveexec_b64 s[8:9], vcc
	s_cbranch_execz .LBB0_952
	v_mov_b32_e32 v1, 0
	global_load_dword v2, v1, s[10:11] offset:-256 sc1
	s_mov_b64 s[28:29], 0
	s_waitcnt vmcnt(0)
	v_cmp_lt_u32_e32 vcc, v2, v19
	s_and_saveexec_b64 s[16:17], vcc
	s_cbranch_execz .LBB0_951
	s_add_u32 s12, s22, 0xc200
	s_addc_u32 s13, s23, 0
	s_mov_b32 s14, 1
	s_branch .LBB0_927

.LBB0_929:
	global_load_dword v2, v1, s[10:11] offset:-256 sc1
	s_add_i32 s14, s14, 1
	s_mov_b64 s[34:35], -1
	s_waitcnt vmcnt(0)
	v_cmp_ge_u32_e32 vcc, v2, v19
	s_orn2_b64 s[38:39], vcc, exec
	s_branch .LBB0_926

; __device__ __forceinline__ unsigned xb_ld(unsigned* p)              { return __hip_atomic_load(p, __ATOMIC_RELAXED, __HIP_MEMORY_SCOPE_AGENT); }
; __device__ __forceinline__ unsigned xb_add(unsigned* p, unsigned v) { return __hip_atomic_fetch_add(p, v, __ATOMIC_RELAXED, __HIP_MEMORY_SCOPE_AGENT); }
; #define XB_SPIN(cond, bar) do { unsigned _sp = 0; while (cond) { __builtin_amdgcn_s_sleep(1); \
;     if ((++_sp & 255u) == 0u) { if (xb_ld(&(bar)[XB_TMO])) break; if (_sp > XB_SPIN_CAP) { atomicAdd(&(bar)[XB_TMO], 1u); break; } } } } while (0)
; __device__ __forceinline__ void xcd_barrier(const XcdBarrier& b) {
;     ...
;         const unsigned gen = old / nloc;
;         if (old + 1u == (gen + 1u) * nloc) {
;             __builtin_amdgcn_fence(__ATOMIC_RELEASE, "agent");
;             asm volatile("s_waitcnt vmcnt(0)" ::: "memory");
;             const unsigned og = xb_add(&bar[XB_TOP], 1u);
;             const unsigned tg = og / nx;
;             if (og + 1u == (tg + 1u) * nx) xb_add(&bar[XB_TOPGEN], 1u);
;             else XB_SPIN(xb_ld(&bar[XB_TOPGEN]) == tg, bar);
;             __builtin_amdgcn_fence(__ATOMIC_ACQUIRE, "agent");
;             xb_add(&bar[XB_XGEN(b.x)], 1u);
;             asm volatile("s_waitcnt vmcnt(0)" ::: "memory");
;         } else {
;             XB_SPIN(xb_ld(&bar[XB_XGEN(b.x)]) == gen, bar);
.LBB0_940:
	s_or_b64 exec, exec, s[12:13]
	v_cvt_f32_u32_e32 v5, v3
	s_waitcnt vmcnt(1)
	v_readfirstlane_b32 s10, v4
	v_sub_u32_e32 v4, 0, v3
	v_rcp_iflag_f32_e32 v5, v5
	v_add_u32_e32 v6, s10, v2
	v_mul_f32_e32 v5, 0x4f7ffffe, v5
	v_cvt_u32_f32_e32 v5, v5
	v_mul_lo_u32 v2, v4, v5
	v_mul_hi_u32 v2, v5, v2
	v_add_u32_e32 v2, v5, v2
	v_mul_hi_u32 v2, v6, v2
	v_mul_lo_u32 v4, v2, v3
	v_sub_u32_e32 v4, v6, v4
	v_add_u32_e32 v5, 1, v2
	v_cmp_ge_u32_e32 vcc, v4, v3
	s_nop 1
	v_cndmask_b32_e32 v2, v2, v5, vcc
	v_sub_u32_e32 v5, v4, v3
	v_cndmask_b32_e32 v4, v4, v5, vcc
	v_add_u32_e32 v5, 1, v2
	v_cmp_ge_u32_e32 vcc, v4, v3
	v_add_u32_e32 v4, 1, v6
	s_nop 0
	v_cndmask_b32_e32 v2, v2, v5, vcc
	v_mul_lo_u32 v5, v3, v2
	v_add_u32_e32 v3, v5, v3
	v_cmp_ne_u32_e32 vcc, v4, v3
	s_and_saveexec_b64 s[10:11], vcc
	s_xor_b64 s[10:11], exec, s[10:11]
	s_cbranch_execz .LBB0_1585
	s_waitcnt lgkmcnt(0)
	v_mov_b32_e32 v20, 0x23824
	ds_read_b32 v20, v20
	v_add_u32_e32 v21, 1, v2
	s_waitcnt lgkmcnt(0)
	v_mul_lo_u32 v21, v21, v20
	v_mov_b32_e32 v1, 0
	s_lshl_b32 s99, s33, 8
	s_sub_u32 s30, s8, s99
	s_subb_u32 s31, s9, 0
	s_add_u32 s30, s30, 0x3400
	s_addc_u32 s31, s31, 0
	global_load_dword v1, v1, s[30:31] sc1
	s_waitcnt vmcnt(0)
	v_cmp_lt_u32_e32 vcc, v1, v21
	s_and_saveexec_b64 s[12:13], vcc
	s_cbranch_execz .LBB0_1584
	s_add_u32 s28, s22, 0x4200
	s_addc_u32 s29, s23, 0
	s_mov_b32 s14, 1
	s_mov_b64 s[34:35], 0
	v_mov_b32_e32 v1, 0
	s_branch .LBB0_944

.LBB0_946:
	global_load_dword v3, v1, s[30:31] sc1
	s_add_i32 s14, s14, 1
	s_mov_b64 s[40:41], -1
	s_waitcnt vmcnt(0)
	v_cmp_ge_u32_e32 vcc, v3, v21
	s_orn2_b64 s[38:39], vcc, exec
	s_branch .LBB0_943

; __device__ __forceinline__ unsigned xb_ld(unsigned* p)              { return __hip_atomic_load(p, __ATOMIC_RELAXED, __HIP_MEMORY_SCOPE_AGENT); }
; __device__ __forceinline__ unsigned xb_add(unsigned* p, unsigned v) { return __hip_atomic_fetch_add(p, v, __ATOMIC_RELAXED, __HIP_MEMORY_SCOPE_AGENT); }
; #define XB_SPIN(cond, bar) do { unsigned _sp = 0; while (cond) { __builtin_amdgcn_s_sleep(1); \
;     if ((++_sp & 255u) == 0u) { if (xb_ld(&(bar)[XB_TMO])) break; if (_sp > XB_SPIN_CAP) { atomicAdd(&(bar)[XB_TMO], 1u); break; } } } } while (0)
; __device__ __forceinline__ void xcd_barrier(const XcdBarrier& b) {
;     ...
;         const unsigned gen = old / nloc;
;         if (old + 1u == (gen + 1u) * nloc) {
;             __builtin_amdgcn_fence(__ATOMIC_RELEASE, "agent");
;             asm volatile("s_waitcnt vmcnt(0)" ::: "memory");
;             const unsigned og = xb_add(&bar[XB_TOP], 1u);
;             const unsigned tg = og / nx;
;             if (og + 1u == (tg + 1u) * nx) xb_add(&bar[XB_TOPGEN], 1u);
;             else XB_SPIN(xb_ld(&bar[XB_TOPGEN]) == tg, bar);
;             __builtin_amdgcn_fence(__ATOMIC_ACQUIRE, "agent");
;             xb_add(&bar[XB_XGEN(b.x)], 1u);
;             asm volatile("s_waitcnt vmcnt(0)" ::: "memory");
;         } else {
;             XB_SPIN(xb_ld(&bar[XB_XGEN(b.x)]) == gen, bar);
.LBB0_1043:
	s_or_b64 exec, exec, s[12:13]
	v_cvt_f32_u32_e32 v5, v3
	s_waitcnt vmcnt(1)
	v_readfirstlane_b32 s10, v4
	v_sub_u32_e32 v4, 0, v3
	v_rcp_iflag_f32_e32 v5, v5
	v_add_u32_e32 v6, s10, v2
	v_mul_f32_e32 v5, 0x4f7ffffe, v5
	v_cvt_u32_f32_e32 v5, v5
	v_mul_lo_u32 v2, v4, v5
	v_mul_hi_u32 v2, v5, v2
	v_add_u32_e32 v2, v5, v2
	v_mul_hi_u32 v2, v6, v2
	v_mul_lo_u32 v4, v2, v3
	v_sub_u32_e32 v4, v6, v4
	v_add_u32_e32 v5, 1, v2
	v_cmp_ge_u32_e32 vcc, v4, v3
	s_nop 1
	v_cndmask_b32_e32 v2, v2, v5, vcc
	v_sub_u32_e32 v5, v4, v3
	v_cndmask_b32_e32 v4, v4, v5, vcc
	v_add_u32_e32 v5, 1, v2
	v_cmp_ge_u32_e32 vcc, v4, v3
	v_add_u32_e32 v4, 1, v6
	s_nop 0
	v_cndmask_b32_e32 v2, v2, v5, vcc
	v_mul_lo_u32 v5, v3, v2
	v_add_u32_e32 v3, v5, v3
	v_cmp_ne_u32_e32 vcc, v4, v3
	s_and_saveexec_b64 s[10:11], vcc
	s_xor_b64 s[10:11], exec, s[10:11]
	s_cbranch_execz .LBB0_1057
	s_waitcnt lgkmcnt(0)
	v_mov_b32_e32 v20, 0x23824
	ds_read_b32 v20, v20
	v_add_u32_e32 v21, 1, v2
	s_waitcnt lgkmcnt(0)
	v_mul_lo_u32 v21, v21, v20
	v_mov_b32_e32 v1, 0
	s_lshl_b32 s99, s33, 8
	s_sub_u32 s16, s8, s99
	s_subb_u32 s17, s9, 0
	s_add_u32 s16, s16, 0x3400
	s_addc_u32 s17, s17, 0
	global_load_dword v1, v1, s[16:17] sc1
	s_waitcnt vmcnt(0)
	v_cmp_lt_u32_e32 vcc, v1, v21
	s_and_saveexec_b64 s[12:13], vcc
	s_cbranch_execz .LBB0_1056
	s_add_u32 s14, s22, 0x4200
	s_addc_u32 s15, s23, 0
	s_mov_b32 s18, 1
	s_mov_b64 s[28:29], 0
	v_mov_b32_e32 v1, 0
	s_branch .LBB0_1047

.LBB0_1049:
	global_load_dword v3, v1, s[16:17] sc1
	s_add_i32 s18, s18, 1
	s_mov_b64 s[36:37], -1
	s_waitcnt vmcnt(0)
	v_cmp_ge_u32_e32 vcc, v3, v21
	s_orn2_b64 s[34:35], vcc, exec
	s_branch .LBB0_1046

; __device__ __forceinline__ unsigned xb_ld(unsigned* p)              { return __hip_atomic_load(p, __ATOMIC_RELAXED, __HIP_MEMORY_SCOPE_AGENT); }
; __device__ __forceinline__ unsigned xb_add(unsigned* p, unsigned v) { return __hip_atomic_fetch_add(p, v, __ATOMIC_RELAXED, __HIP_MEMORY_SCOPE_AGENT); }
; #define XB_SPIN(cond, bar) do { unsigned _sp = 0; while (cond) { __builtin_amdgcn_s_sleep(1); \
;     if ((++_sp & 255u) == 0u) { if (xb_ld(&(bar)[XB_TMO])) break; if (_sp > XB_SPIN_CAP) { atomicAdd(&(bar)[XB_TMO], 1u); break; } } } } while (0)
; __device__ __forceinline__ void xcd_barrier(const XcdBarrier& b) {
;     ...
;             const unsigned og = xb_add(&bar[XB_TOP], 1u);
;             const unsigned tg = og / nx;
;             if (og + 1u == (tg + 1u) * nx) xb_add(&bar[XB_TOPGEN], 1u);
;             else XB_SPIN(xb_ld(&bar[XB_TOPGEN]) == tg, bar);
.LBB0_1060:
	s_or_b64 exec, exec, s[12:13]
	v_cvt_f32_u32_e32 v4, v1
	s_waitcnt vmcnt(0)
	v_readfirstlane_b32 s10, v3
	s_add_u32 s12, s22, 0x7500
	s_addc_u32 s13, s23, 0
	v_rcp_iflag_f32_e32 v4, v4
	v_add_u32_e32 v2, s10, v2
	v_add_u32_e32 v5, 1, v2
	s_mov_b64 s[14:15], -1
	v_mul_f32_e32 v3, 0x4f7ffffe, v4
	v_cvt_u32_f32_e32 v3, v3
	v_sub_u32_e32 v4, 0, v1
	v_mul_lo_u32 v4, v4, v3
	v_mul_hi_u32 v4, v3, v4
	v_add_u32_e32 v3, v3, v4
	v_mul_hi_u32 v3, v2, v3
	v_mul_lo_u32 v4, v3, v1
	v_sub_u32_e32 v2, v2, v4
	v_add_u32_e32 v6, 1, v3
	v_cmp_ge_u32_e32 vcc, v2, v1
	v_sub_u32_e32 v4, v2, v1
	s_nop 0
	v_cndmask_b32_e32 v3, v3, v6, vcc
	v_cndmask_b32_e32 v2, v2, v4, vcc
	v_add_u32_e32 v4, 1, v3
	v_cmp_ge_u32_e32 vcc, v2, v1
	s_nop 1
	v_cndmask_b32_e32 v4, v3, v4, vcc
	v_mul_lo_u32 v2, v1, v4
	v_add_u32_e32 v1, v2, v1
	v_mov_b32_e32 v19, v1
	v_cmp_ne_u32_e32 vcc, v5, v1
	v_mov_b64_e32 v[2:3], s[12:13]
	s_and_saveexec_b64 s[10:11], vcc
	s_cbranch_execz .LBB0_1072
	v_mov_b32_e32 v1, 0
	global_load_dword v2, v1, s[12:13] offset:-256 sc1
	s_mov_b64 s[28:29], 0
	s_waitcnt vmcnt(0)
	v_cmp_lt_u32_e32 vcc, v2, v19
	s_and_saveexec_b64 s[16:17], vcc
	s_cbranch_execz .LBB0_1071
	s_add_u32 s14, s22, 0x4200
	s_addc_u32 s15, s23, 0
	s_mov_b32 s18, 1
	s_branch .LBB0_1064

.LBB0_1066:
	global_load_dword v2, v1, s[12:13] offset:-256 sc1
	s_add_i32 s18, s18, 1
	s_mov_b64 s[34:35], -1
	s_waitcnt vmcnt(0)
	v_cmp_ge_u32_e32 vcc, v2, v19
	s_orn2_b64 s[38:39], vcc, exec
	s_branch .LBB0_1063

; __device__ __forceinline__ unsigned xb_ld(unsigned* p)              { return __hip_atomic_load(p, __ATOMIC_RELAXED, __HIP_MEMORY_SCOPE_AGENT); }
; __device__ __forceinline__ unsigned xb_add(unsigned* p, unsigned v) { return __hip_atomic_fetch_add(p, v, __ATOMIC_RELAXED, __HIP_MEMORY_SCOPE_AGENT); }
; #define XB_SPIN(cond, bar) do { unsigned _sp = 0; while (cond) { __builtin_amdgcn_s_sleep(1); \
;     if ((++_sp & 255u) == 0u) { if (xb_ld(&(bar)[XB_TMO])) break; if (_sp > XB_SPIN_CAP) { atomicAdd(&(bar)[XB_TMO], 1u); break; } } } } while (0)
; __device__ __forceinline__ void xcd_barrier(const XcdBarrier& b) {
;     ...
;         const unsigned gen = old / nloc;
;         if (old + 1u == (gen + 1u) * nloc) {
;             __builtin_amdgcn_fence(__ATOMIC_RELEASE, "agent");
;             asm volatile("s_waitcnt vmcnt(0)" ::: "memory");
;             const unsigned og = xb_add(&bar[XB_TOP], 1u);
;             const unsigned tg = og / nx;
;             if (og + 1u == (tg + 1u) * nx) xb_add(&bar[XB_TOPGEN], 1u);
;             else XB_SPIN(xb_ld(&bar[XB_TOPGEN]) == tg, bar);
;             __builtin_amdgcn_fence(__ATOMIC_ACQUIRE, "agent");
;             xb_add(&bar[XB_XGEN(b.x)], 1u);
;             asm volatile("s_waitcnt vmcnt(0)" ::: "memory");
;         } else {
;             XB_SPIN(xb_ld(&bar[XB_XGEN(b.x)]) == gen, bar);
.LBB0_1541:
	s_or_b64 exec, exec, s[12:13]
	v_cvt_f32_u32_e32 v5, v3
	s_waitcnt vmcnt(1)
	v_readfirstlane_b32 s1, v4
	v_sub_u32_e32 v4, 0, v3
	v_rcp_iflag_f32_e32 v5, v5
	v_add_u32_e32 v6, s1, v2
	v_mul_f32_e32 v5, 0x4f7ffffe, v5
	v_cvt_u32_f32_e32 v5, v5
	v_mul_lo_u32 v2, v4, v5
	v_mul_hi_u32 v2, v5, v2
	v_add_u32_e32 v2, v5, v2
	v_mul_hi_u32 v2, v6, v2
	v_mul_lo_u32 v4, v2, v3
	v_sub_u32_e32 v4, v6, v4
	v_add_u32_e32 v5, 1, v2
	v_cmp_ge_u32_e32 vcc, v4, v3
	s_nop 1
	v_cndmask_b32_e32 v2, v2, v5, vcc
	v_sub_u32_e32 v5, v4, v3
	v_cndmask_b32_e32 v4, v4, v5, vcc
	v_add_u32_e32 v5, 1, v2
	v_cmp_ge_u32_e32 vcc, v4, v3
	v_add_u32_e32 v4, 1, v6
	s_nop 0
	v_cndmask_b32_e32 v2, v2, v5, vcc
	v_mul_lo_u32 v5, v3, v2
	v_add_u32_e32 v3, v5, v3
	v_cmp_ne_u32_e32 vcc, v4, v3
	s_and_saveexec_b64 s[10:11], vcc
	s_xor_b64 s[10:11], exec, s[10:11]
	s_cbranch_execz .LBB0_1555
	s_waitcnt lgkmcnt(0)
	v_mov_b32_e32 v20, 0x23824
	ds_read_b32 v20, v20
	v_add_u32_e32 v21, 1, v2
	s_waitcnt lgkmcnt(0)
	v_mul_lo_u32 v21, v21, v20
	v_mov_b32_e32 v1, 0
	s_lshl_b32 s99, s33, 8
	s_sub_u32 s16, s8, s99
	s_subb_u32 s17, s9, 0
	s_add_u32 s16, s16, 0x3400
	s_addc_u32 s17, s17, 0
	global_load_dword v1, v1, s[16:17] sc1
	s_waitcnt vmcnt(0)
	v_cmp_lt_u32_e32 vcc, v1, v21
	s_and_saveexec_b64 s[12:13], vcc
	s_cbranch_execz .LBB0_1554
	s_add_u32 s14, s22, 0x4200
	s_addc_u32 s15, s23, 0
	s_mov_b32 s1, 1
	s_mov_b64 s[18:19], 0
	v_mov_b32_e32 v1, 0
	s_branch .LBB0_1545

.LBB0_1547:
	global_load_dword v3, v1, s[16:17] sc1
	s_add_i32 s1, s1, 1
	s_mov_b64 s[28:29], -1
	s_waitcnt vmcnt(0)
	v_cmp_ge_u32_e32 vcc, v3, v21
	s_orn2_b64 s[26:27], vcc, exec
	s_branch .LBB0_1544

; __device__ __forceinline__ unsigned xb_ld(unsigned* p)              { return __hip_atomic_load(p, __ATOMIC_RELAXED, __HIP_MEMORY_SCOPE_AGENT); }
; __device__ __forceinline__ unsigned xb_add(unsigned* p, unsigned v) { return __hip_atomic_fetch_add(p, v, __ATOMIC_RELAXED, __HIP_MEMORY_SCOPE_AGENT); }
; #define XB_SPIN(cond, bar) do { unsigned _sp = 0; while (cond) { __builtin_amdgcn_s_sleep(1); \
;     if ((++_sp & 255u) == 0u) { if (xb_ld(&(bar)[XB_TMO])) break; if (_sp > XB_SPIN_CAP) { atomicAdd(&(bar)[XB_TMO], 1u); break; } } } } while (0)
; __device__ __forceinline__ void xcd_barrier(const XcdBarrier& b) {
;     ...
;             const unsigned og = xb_add(&bar[XB_TOP], 1u);
;             const unsigned tg = og / nx;
;             if (og + 1u == (tg + 1u) * nx) xb_add(&bar[XB_TOPGEN], 1u);
;             else XB_SPIN(xb_ld(&bar[XB_TOPGEN]) == tg, bar);
.LBB0_1558:
	s_or_b64 exec, exec, s[12:13]
	v_cvt_f32_u32_e32 v4, v1
	s_waitcnt vmcnt(0)
	v_readfirstlane_b32 s1, v3
	s_add_u32 s12, s22, 0x7500
	s_addc_u32 s13, s23, 0
	v_rcp_iflag_f32_e32 v4, v4
	v_add_u32_e32 v2, s1, v2
	v_add_u32_e32 v5, 1, v2
	s_mov_b64 s[14:15], -1
	v_mul_f32_e32 v3, 0x4f7ffffe, v4
	v_cvt_u32_f32_e32 v3, v3
	v_sub_u32_e32 v4, 0, v1
	v_mul_lo_u32 v4, v4, v3
	v_mul_hi_u32 v4, v3, v4
	v_add_u32_e32 v3, v3, v4
	v_mul_hi_u32 v3, v2, v3
	v_mul_lo_u32 v4, v3, v1
	v_sub_u32_e32 v2, v2, v4
	v_add_u32_e32 v6, 1, v3
	v_cmp_ge_u32_e32 vcc, v2, v1
	v_sub_u32_e32 v4, v2, v1
	s_nop 0
	v_cndmask_b32_e32 v3, v3, v6, vcc
	v_cndmask_b32_e32 v2, v2, v4, vcc
	v_add_u32_e32 v4, 1, v3
	v_cmp_ge_u32_e32 vcc, v2, v1
	s_nop 1
	v_cndmask_b32_e32 v4, v3, v4, vcc
	v_mul_lo_u32 v2, v1, v4
	v_add_u32_e32 v1, v2, v1
	v_mov_b32_e32 v19, v1
	v_cmp_ne_u32_e32 vcc, v5, v1
	v_mov_b64_e32 v[2:3], s[12:13]
	s_and_saveexec_b64 s[10:11], vcc
	s_cbranch_execz .LBB0_1570
	v_mov_b32_e32 v1, 0
	global_load_dword v2, v1, s[12:13] offset:-256 sc1
	s_mov_b64 s[18:19], 0
	s_waitcnt vmcnt(0)
	v_cmp_lt_u32_e32 vcc, v2, v19
	s_and_saveexec_b64 s[16:17], vcc
	s_cbranch_execz .LBB0_1569
	s_add_u32 s14, s22, 0x4200
	s_addc_u32 s15, s23, 0
	s_mov_b32 s1, 1
	s_branch .LBB0_1562

; __device__ __forceinline__ unsigned xb_ld(unsigned* p)              { return __hip_atomic_load(p, __ATOMIC_RELAXED, __HIP_MEMORY_SCOPE_AGENT); }
; __device__ __forceinline__ unsigned xb_add(unsigned* p, unsigned v) { return __hip_atomic_fetch_add(p, v, __ATOMIC_RELAXED, __HIP_MEMORY_SCOPE_AGENT); }
; #define XB_SPIN(cond, bar) do { unsigned _sp = 0; while (cond) { __builtin_amdgcn_s_sleep(1); \
;     if ((++_sp & 255u) == 0u) { if (xb_ld(&(bar)[XB_TMO])) break; if (_sp > XB_SPIN_CAP) { atomicAdd(&(bar)[XB_TMO], 1u); break; } } } } while (0)
; __device__ __forceinline__ void xcd_barrier(const XcdBarrier& b) {
;     ...
;             const unsigned og = xb_add(&bar[XB_TOP], 1u);
;             const unsigned tg = og / nx;
;             if (og + 1u == (tg + 1u) * nx) xb_add(&bar[XB_TOPGEN], 1u);
;             else XB_SPIN(xb_ld(&bar[XB_TOPGEN]) == tg, bar);
.LBB0_1564:
	global_load_dword v2, v1, s[12:13] offset:-256 sc1
	s_add_i32 s1, s1, 1
	s_mov_b64 s[24:25], -1
	s_waitcnt vmcnt(0)
	v_cmp_ge_u32_e32 vcc, v2, v19
	s_orn2_b64 s[28:29], vcc, exec
	s_branch .LBB0_1561

; __device__ __forceinline__ unsigned xb_ld(unsigned* p)              { return __hip_atomic_load(p, __ATOMIC_RELAXED, __HIP_MEMORY_SCOPE_AGENT); }
; __device__ __forceinline__ unsigned xb_add(unsigned* p, unsigned v) { return __hip_atomic_fetch_add(p, v, __ATOMIC_RELAXED, __HIP_MEMORY_SCOPE_AGENT); }
; #define XB_SPIN(cond, bar) do { unsigned _sp = 0; while (cond) { __builtin_amdgcn_s_sleep(1); \
;     if ((++_sp & 255u) == 0u) { if (xb_ld(&(bar)[XB_TMO])) break; if (_sp > XB_SPIN_CAP) { atomicAdd(&(bar)[XB_TMO], 1u); break; } } } } while (0)
; __device__ __forceinline__ void xcd_barrier(const XcdBarrier& b) {
;     ...
;         const unsigned old = xb_add(&bar[XB_XSUB(b.x)], 1u);
;         const unsigned gen = old / nloc;
;         if (old + 1u == (gen + 1u) * nloc) {
;             __builtin_amdgcn_fence(__ATOMIC_RELEASE, "agent");
;             asm volatile("s_waitcnt vmcnt(0)" ::: "memory");
;             const unsigned og = xb_add(&bar[XB_TOP], 1u);
;             const unsigned tg = og / nx;
;             if (og + 1u == (tg + 1u) * nx) xb_add(&bar[XB_TOPGEN], 1u);
;             else XB_SPIN(xb_ld(&bar[XB_TOPGEN]) == tg, bar);
.LBB0_1588:
	s_or_b64 exec, exec, s[12:13]
	v_cvt_f32_u32_e32 v4, v1
	s_waitcnt vmcnt(0)
	v_readfirstlane_b32 s10, v3
	s_add_u32 s12, s22, 0x7500
	s_addc_u32 s13, s23, 0
	v_rcp_iflag_f32_e32 v4, v4
	v_add_u32_e32 v2, s10, v2
	v_add_u32_e32 v5, 1, v2
	s_mov_b64 s[28:29], -1
	v_mul_f32_e32 v3, 0x4f7ffffe, v4
	v_cvt_u32_f32_e32 v3, v3
	v_sub_u32_e32 v4, 0, v1
	v_mul_lo_u32 v4, v4, v3
	v_mul_hi_u32 v4, v3, v4
	v_add_u32_e32 v3, v3, v4
	v_mul_hi_u32 v3, v2, v3
	v_mul_lo_u32 v4, v3, v1
	v_sub_u32_e32 v2, v2, v4
	v_add_u32_e32 v6, 1, v3
	v_cmp_ge_u32_e32 vcc, v2, v1
	v_sub_u32_e32 v4, v2, v1
	s_nop 0
	v_cndmask_b32_e32 v3, v3, v6, vcc
	v_cndmask_b32_e32 v2, v2, v4, vcc
	v_add_u32_e32 v4, 1, v3
	v_cmp_ge_u32_e32 vcc, v2, v1
	s_nop 1
	v_cndmask_b32_e32 v4, v3, v4, vcc
	v_mul_lo_u32 v2, v1, v4
	v_add_u32_e32 v1, v2, v1
	v_mov_b32_e32 v19, v1
	v_cmp_ne_u32_e32 vcc, v5, v1
	v_mov_b64_e32 v[2:3], s[12:13]
	s_and_saveexec_b64 s[10:11], vcc
	s_cbranch_execz .LBB0_1600
	v_mov_b32_e32 v1, 0
	global_load_dword v2, v1, s[12:13] offset:-256 sc1
	s_mov_b64 s[34:35], 0
	s_waitcnt vmcnt(0)
	v_cmp_lt_u32_e32 vcc, v2, v19
	s_and_saveexec_b64 s[30:31], vcc
	s_cbranch_execz .LBB0_1599
	s_add_u32 s28, s22, 0x4200
	s_addc_u32 s29, s23, 0
	s_mov_b32 s14, 1
	s_branch .LBB0_1592

; __device__ __forceinline__ unsigned xb_ld(unsigned* p)              { return __hip_atomic_load(p, __ATOMIC_RELAXED, __HIP_MEMORY_SCOPE_AGENT); }
; #define XB_SPIN(cond, bar) do { unsigned _sp = 0; while (cond) { __builtin_amdgcn_s_sleep(1); \
;     if ((++_sp & 255u) == 0u) { if (xb_ld(&(bar)[XB_TMO])) break; if (_sp > XB_SPIN_CAP) { atomicAdd(&(bar)[XB_TMO], 1u); break; } } } } while (0)
; __device__ __forceinline__ void xcd_barrier(const XcdBarrier& b) {
;     ...
;             else XB_SPIN(xb_ld(&bar[XB_TOPGEN]) == tg, bar);
.LBB0_1594:
	global_load_dword v2, v1, s[12:13] offset:-256 sc1
	s_add_i32 s14, s14, 1
	s_mov_b64 s[38:39], -1
	s_waitcnt vmcnt(0)
	v_cmp_ge_u32_e32 vcc, v2, v19
	s_orn2_b64 s[42:43], vcc, exec
	s_branch .LBB0_1591
